# expert weight conversion hosted inside the grid barriers (waves 1-7, one 64x64 tile per barrier) and in the attention phase (wave 0 all tiles, waves 1-7 four tiles)
# speedup vs baseline: 1.0547x; 1.0028x over previous
.LBB0_11:
	s_or_b64 exec, exec, s[4:5]
	s_load_dwordx16 s[4:19], s[0:1], 0x40
	s_lshl_b32 s26, s74, 3
	s_lshl_b32 s0, s96, 3
	v_readlane_b32 s98, v239, 0
	s_lshr_b32 s98, s98, 6
	s_add_i32 s98, s98, s0
	s_add_i32 s98, s98, 2048
	v_writelane_b32 v239, s62, 44
	v_writelane_b32 v239, s63, 45
	s_cmp_lt_i32 s64, 1
	s_waitcnt lgkmcnt(0)
	v_writelane_b32 v239, s4, 7
	s_nop 1
	v_writelane_b32 v239, s5, 8
	v_writelane_b32 v239, s6, 9
	v_writelane_b32 v239, s7, 10
	v_writelane_b32 v239, s8, 11
	v_writelane_b32 v239, s9, 12
	v_writelane_b32 v239, s10, 13
	v_writelane_b32 v239, s11, 14
	v_writelane_b32 v239, s12, 15
	v_writelane_b32 v239, s13, 16
	v_writelane_b32 v239, s14, 17
	v_writelane_b32 v239, s15, 18
	v_writelane_b32 v239, s16, 19
	v_writelane_b32 v239, s17, 20
	v_writelane_b32 v239, s18, 21
	v_writelane_b32 v239, s19, 22
	v_writelane_b32 v239, s0, 23
	s_cselect_b64 s[0:1], -1, 0
	s_cmp_gt_i32 s65, 0
	s_cselect_b64 s[2:3], -1, 0
	s_and_b64 s[4:5], s[0:1], s[2:3]
	s_andn2_b64 vcc, exec, s[4:5]
	s_cbranch_vccnz .LBB0_54
	v_mov_b32_e32 v2, v0
	s_mov_b32 s0, 0x10000
	v_mul_lo_u32 v1, v2, s74
	v_add_u32_e32 v1, s96, v1
	v_readfirstlane_b32 s2, v2
	v_cmp_gt_i32_e32 vcc, s0, v1
	s_and_saveexec_b64 s[6:7], vcc
	s_cbranch_execz .LBB0_15
	v_and_b32_e32 v4, 31, v1
	s_mov_b32 s0, 0x979a371
	v_cvt_f64_u32_e32 v[4:5], v4
	s_mov_b32 s1, 0xbfda934f
	v_mul_f64 v[4:5], v[4:5], s[0:1]
	v_rndne_f64_e32 v[6:7], v[4:5]
	s_mov_b32 s0, 0x3b39803f
	v_add_f64 v[8:9], v[4:5], -v[6:7]
	s_mov_b32 s1, 0x3c7abc9e
	v_mul_f64 v[10:11], v[8:9], s[0:1]
	s_mov_b32 s0, 0xfefa39ef
	s_mov_b32 s1, 0x3fe62e42
	v_fmac_f64_e32 v[10:11], s[0:1], v[8:9]
	s_mov_b32 s0, 0x6a5dcb37
	v_mov_b32_e32 v8, 0xfca7ab0c
	v_mov_b32_e32 v9, 0x3e928af3
	s_mov_b32 s1, 0x3e5ade15
	v_fmac_f64_e32 v[8:9], s[0:1], v[10:11]
	v_mov_b32_e32 v12, 0x623fde64
	v_mov_b32_e32 v13, 0x3ec71dee
	v_fmac_f64_e32 v[12:13], v[10:11], v[8:9]
	v_mov_b32_e32 v8, 0x7c89e6b0
	v_mov_b32_e32 v9, 0x3efa0199
	v_fmac_f64_e32 v[8:9], v[10:11], v[12:13]
	v_mov_b32_e32 v12, 0x14761f6e
	v_mov_b32_e32 v13, 0x3f2a01a0
	v_fmac_f64_e32 v[12:13], v[10:11], v[8:9]
	v_mov_b32_e32 v8, 0x1852b7b0
	v_mov_b32_e32 v9, 0x3f56c16c
	v_fmac_f64_e32 v[8:9], v[10:11], v[12:13]
	v_mov_b32_e32 v12, 0x11122322
	v_mov_b32_e32 v13, 0x3f811111
	v_fmac_f64_e32 v[12:13], v[10:11], v[8:9]
	v_mov_b32_e32 v8, 0x555502a1
	v_mov_b32_e32 v9, 0x3fa55555
	v_fmac_f64_e32 v[8:9], v[10:11], v[12:13]
	v_mov_b32_e32 v12, 0x55555511
	v_mov_b32_e32 v13, 0x3fc55555
	v_fmac_f64_e32 v[12:13], v[10:11], v[8:9]
	v_mov_b32_e32 v8, 11
	v_mov_b32_e32 v9, 0x3fe00000
	s_mov_b32 s0, 0
	v_fmac_f64_e32 v[8:9], v[10:11], v[12:13]
	s_mov_b32 s1, 0x40900000
	v_fma_f64 v[8:9], v[10:11], v[8:9], 1.0
	v_cmp_nlt_f64_e32 vcc, s[0:1], v[4:5]
	s_mov_b32 s0, 0
	v_fma_f64 v[8:9], v[10:11], v[8:9], 1.0
	v_cvt_i32_f64_e32 v6, v[6:7]
	s_mov_b32 s1, 0xc090cc00
	s_add_u32 s8, s62, 0x100000
	v_ldexp_f64 v[6:7], v[8:9], v6
	v_mov_b32_e32 v8, 0x7ff00000
	v_cmp_ngt_f64_e64 s[0:1], s[0:1], v[4:5]
	s_addc_u32 s9, s63, 0
	v_cndmask_b32_e32 v7, v8, v7, vcc
	s_and_b64 vcc, s[0:1], vcc
	s_mov_b32 s10, 0x6dc9c883
	s_mov_b32 s12, 0x54442d18
	s_lshl_b32 s3, s74, 9
	v_and_b32_e32 v3, 3, v1
	v_cndmask_b32_e64 v5, 0, v7, s[0:1]
	v_cndmask_b32_e32 v4, 0, v6, vcc
	v_bfe_u32 v6, v1, 3, 2
	v_lshlrev_b32_e32 v7, 13, v1
	s_lshl_b32 s15, s74, 22
	s_mov_b64 s[0:1], 0
	s_mov_b32 s11, 0x3fc45f30
	s_mov_b32 s13, 0xc01921fb
	s_mov_b32 s14, 0x3d000000
	s_mov_b32 s16, 0x3fffffc
	s_mov_b32 s17, 0xffff

.LBB0_258:
	s_cmp_lg_u32 s35, 0
	s_cselect_b64 s[66:67], -1, 0
	s_min_i32 s0, s3, 4
	s_add_i32 s2, s0, s20
	s_cmp_eq_u32 s35, 0
	s_cselect_b64 s[86:87], -1, 0
	s_and_b64 s[0:1], s[86:87], exec
	s_cselect_b32 s0, s2, 8
	s_mov_b32 s99, 0
	s_cmp_gt_u32 s98, 26623
	s_cbranch_scc1 .Lhw_x_skip
	s_sub_i32 s23, s98, 2048
	s_and_b32 s32, s23, 7
	s_cmp_eq_u32 s32, 0
	s_cbranch_scc1 .Lhw_x_go
	s_lshr_b32 s32, s23, 11
	s_cmp_lt_u32 s32, 6
	s_cbranch_scc0 .Lhw_x_skip
.Lhw_x_go:
	s_mov_b32 s99, 1
	v_mbcnt_lo_u32_b32 v178, -1, 0
	v_mbcnt_hi_u32_b32 v178, -1, v178
	v_and_b32_e32 v179, 60, v178
	v_lshlrev_b32_e32 v179, 10, v179
	v_and_b32_e32 v180, 3, v178
	v_lshl_or_b32 v179, v180, 4, v179
	v_add_u32_e32 v180, 0x400, v179
	v_add_u32_e32 v181, 0x800, v179
	v_add_u32_e32 v190, 0xc00, v179
	v_lshlrev_b32_e32 v178, 2, v178
	s_sub_i32 s23, s98, 2048
	s_cmp_lt_u32 s23, 16384
	s_cbranch_scc0 .Lhw_dn_a
	s_lshr_b32 s29, s23, 9
	s_bfe_u32 s24, s23, 0x40005
	s_and_b32 s25, s23, 31
	s_lshl_b32 s30, s29, 23
	s_lshl_b32 s32, s24, 19
	s_add_i32 s30, s30, s32
	s_lshl_b32 s32, s25, 8
	s_add_i32 s30, s30, s32
	s_lshl_b32 s31, s29, 11
	s_bfe_u32 s32, s25, 0x30001
	s_lshl_b32 s32, s32, 8
	s_add_i32 s31, s31, s32
	s_lshr_b32 s32, s25, 4
	s_lshl_b32 s32, s32, 7
	s_add_i32 s31, s31, s32
	s_and_b32 s32, s25, 1
	s_lshl_b32 s32, s32, 6
	s_add_i32 s31, s31, s32
	s_lshl_b32 s31, s31, 10
	s_lshl_b32 s32, s24, 6
	s_add_i32 s31, s31, s32
	s_add_i32 s31, s31, 0x2000000
	v_readlane_b32 s82, v239, 11
	v_readlane_b32 s83, v239, 12
	s_movk_i32 s97, 8192
	s_branch .Lhw_go_a

.Lhw_go_a:
	s_add_u32 s100, s82, s30
	s_addc_u32 s101, s83, 0
	v_readlane_b32 s70, v239, 44
	v_readlane_b32 s71, v239, 45
	s_add_u32 s70, s70, s31
	s_addc_u32 s71, s71, 0
	global_load_dword v34, v178, s[100:101] nt
	s_add_u32 s100, s100, s97
	s_addc_u32 s101, s101, 0
	global_load_dword v35, v178, s[100:101] nt
	s_add_u32 s100, s100, s97
	s_addc_u32 s101, s101, 0
	global_load_dword v36, v178, s[100:101] nt
	s_add_u32 s100, s100, s97
	s_addc_u32 s101, s101, 0
	global_load_dword v37, v178, s[100:101] nt
	s_add_u32 s100, s100, s97
	s_addc_u32 s101, s101, 0
	global_load_dword v38, v178, s[100:101] nt
	s_add_u32 s100, s100, s97
	s_addc_u32 s101, s101, 0
	global_load_dword v39, v178, s[100:101] nt
	s_add_u32 s100, s100, s97
	s_addc_u32 s101, s101, 0
	global_load_dword v40, v178, s[100:101] nt
	s_add_u32 s100, s100, s97
	s_addc_u32 s101, s101, 0
	global_load_dword v41, v178, s[100:101] nt
	s_add_u32 s100, s100, s97
	s_addc_u32 s101, s101, 0
	global_load_dword v42, v178, s[100:101] nt
	s_add_u32 s100, s100, s97
	s_addc_u32 s101, s101, 0
	global_load_dword v43, v178, s[100:101] nt
	s_add_u32 s100, s100, s97
	s_addc_u32 s101, s101, 0
	global_load_dword v44, v178, s[100:101] nt
	s_add_u32 s100, s100, s97
	s_addc_u32 s101, s101, 0
	global_load_dword v45, v178, s[100:101] nt
	s_add_u32 s100, s100, s97
	s_addc_u32 s101, s101, 0
	global_load_dword v46, v178, s[100:101] nt
	s_add_u32 s100, s100, s97
	s_addc_u32 s101, s101, 0
	global_load_dword v47, v178, s[100:101] nt
	s_add_u32 s100, s100, s97
	s_addc_u32 s101, s101, 0
	global_load_dword v48, v178, s[100:101] nt
	s_add_u32 s100, s100, s97
	s_addc_u32 s101, s101, 0
	global_load_dword v49, v178, s[100:101] nt
	s_add_u32 s100, s100, s97
	s_addc_u32 s101, s101, 0
	global_load_dword v50, v178, s[100:101] nt
	s_add_u32 s100, s100, s97
	s_addc_u32 s101, s101, 0
	global_load_dword v51, v178, s[100:101] nt
	s_add_u32 s100, s100, s97
	s_addc_u32 s101, s101, 0
	global_load_dword v52, v178, s[100:101] nt
	s_add_u32 s100, s100, s97
	s_addc_u32 s101, s101, 0
	global_load_dword v53, v178, s[100:101] nt
	s_add_u32 s100, s100, s97
	s_addc_u32 s101, s101, 0
	global_load_dword v54, v178, s[100:101] nt
	s_add_u32 s100, s100, s97
	s_addc_u32 s101, s101, 0
	global_load_dword v55, v178, s[100:101] nt
	s_add_u32 s100, s100, s97
	s_addc_u32 s101, s101, 0
	global_load_dword v56, v178, s[100:101] nt
	s_add_u32 s100, s100, s97
	s_addc_u32 s101, s101, 0
	global_load_dword v57, v178, s[100:101] nt
	s_add_u32 s100, s100, s97
	s_addc_u32 s101, s101, 0
	global_load_dword v58, v178, s[100:101] nt
	s_add_u32 s100, s100, s97
	s_addc_u32 s101, s101, 0
	global_load_dword v59, v178, s[100:101] nt
	s_add_u32 s100, s100, s97
	s_addc_u32 s101, s101, 0
	global_load_dword v60, v178, s[100:101] nt
	s_add_u32 s100, s100, s97
	s_addc_u32 s101, s101, 0
	global_load_dword v61, v178, s[100:101] nt
	s_add_u32 s100, s100, s97
	s_addc_u32 s101, s101, 0
	global_load_dword v62, v178, s[100:101] nt
	s_add_u32 s100, s100, s97
	s_addc_u32 s101, s101, 0
	global_load_dword v63, v178, s[100:101] nt
	s_add_u32 s100, s100, s97
	s_addc_u32 s101, s101, 0
	global_load_dword v64, v178, s[100:101] nt
	s_add_u32 s100, s100, s97
	s_addc_u32 s101, s101, 0
	global_load_dword v65, v178, s[100:101] nt
	s_add_u32 s100, s100, s97
	s_addc_u32 s101, s101, 0
	global_load_dword v66, v178, s[100:101] nt
	s_add_u32 s100, s100, s97
	s_addc_u32 s101, s101, 0
	global_load_dword v67, v178, s[100:101] nt
	s_add_u32 s100, s100, s97
	s_addc_u32 s101, s101, 0
	global_load_dword v68, v178, s[100:101] nt
	s_add_u32 s100, s100, s97
	s_addc_u32 s101, s101, 0
	global_load_dword v69, v178, s[100:101] nt
	s_add_u32 s100, s100, s97
	s_addc_u32 s101, s101, 0
	global_load_dword v70, v178, s[100:101] nt
	s_add_u32 s100, s100, s97
	s_addc_u32 s101, s101, 0
	global_load_dword v71, v178, s[100:101] nt
	s_add_u32 s100, s100, s97
	s_addc_u32 s101, s101, 0
	global_load_dword v72, v178, s[100:101] nt
	s_add_u32 s100, s100, s97
	s_addc_u32 s101, s101, 0
	global_load_dword v73, v178, s[100:101] nt
	s_add_u32 s100, s100, s97
	s_addc_u32 s101, s101, 0
	global_load_dword v74, v178, s[100:101] nt
	s_add_u32 s100, s100, s97
	s_addc_u32 s101, s101, 0
	global_load_dword v75, v178, s[100:101] nt
	s_add_u32 s100, s100, s97
	s_addc_u32 s101, s101, 0
	global_load_dword v76, v178, s[100:101] nt
	s_add_u32 s100, s100, s97
	s_addc_u32 s101, s101, 0
	global_load_dword v77, v178, s[100:101] nt
	s_add_u32 s100, s100, s97
	s_addc_u32 s101, s101, 0
	global_load_dword v78, v178, s[100:101] nt
	s_add_u32 s100, s100, s97
	s_addc_u32 s101, s101, 0
	global_load_dword v79, v178, s[100:101] nt
	s_add_u32 s100, s100, s97
	s_addc_u32 s101, s101, 0
	global_load_dword v80, v178, s[100:101] nt
	s_add_u32 s100, s100, s97
	s_addc_u32 s101, s101, 0
	global_load_dword v81, v178, s[100:101] nt
	s_add_u32 s100, s100, s97
	s_addc_u32 s101, s101, 0
	global_load_dword v82, v178, s[100:101] nt
	s_add_u32 s100, s100, s97
	s_addc_u32 s101, s101, 0
	global_load_dword v83, v178, s[100:101] nt
	s_add_u32 s100, s100, s97
	s_addc_u32 s101, s101, 0
	global_load_dword v84, v178, s[100:101] nt
	s_add_u32 s100, s100, s97
	s_addc_u32 s101, s101, 0
	global_load_dword v85, v178, s[100:101] nt
	s_add_u32 s100, s100, s97
	s_addc_u32 s101, s101, 0
	global_load_dword v86, v178, s[100:101] nt
	s_add_u32 s100, s100, s97
	s_addc_u32 s101, s101, 0
	global_load_dword v87, v178, s[100:101] nt
	s_add_u32 s100, s100, s97
	s_addc_u32 s101, s101, 0
	global_load_dword v88, v178, s[100:101] nt
	s_add_u32 s100, s100, s97
	s_addc_u32 s101, s101, 0
	global_load_dword v89, v178, s[100:101] nt
	s_add_u32 s100, s100, s97
	s_addc_u32 s101, s101, 0
	global_load_dword v90, v178, s[100:101] nt
	s_add_u32 s100, s100, s97
	s_addc_u32 s101, s101, 0
	global_load_dword v91, v178, s[100:101] nt
	s_add_u32 s100, s100, s97
	s_addc_u32 s101, s101, 0
	global_load_dword v92, v178, s[100:101] nt
	s_add_u32 s100, s100, s97
	s_addc_u32 s101, s101, 0
	global_load_dword v93, v178, s[100:101] nt
	s_add_u32 s100, s100, s97
	s_addc_u32 s101, s101, 0
	global_load_dword v94, v178, s[100:101] nt
	s_add_u32 s100, s100, s97
	s_addc_u32 s101, s101, 0
	global_load_dword v95, v178, s[100:101] nt
	s_add_u32 s100, s100, s97
	s_addc_u32 s101, s101, 0
	global_load_dword v96, v178, s[100:101] nt
	s_add_u32 s100, s100, s97
	s_addc_u32 s101, s101, 0
	s_waitcnt vmcnt(63)
	global_load_dword v97, v178, s[100:101] nt
	s_add_u32 s100, s100, s97
	s_addc_u32 s101, s101, 0
	s_branch .Lhw_x_done

.LBB0_350:
.Lhw_tail:
	s_cmp_gt_u32 s98, 26623
	s_cbranch_scc1 .Lhw_tail_done
	s_sub_i32 s23, s98, 2048
	s_and_b32 s32, s23, 7
	s_cmp_eq_u32 s32, 0
	s_cbranch_scc0 .Lhw_tail_done
	v_mbcnt_lo_u32_b32 v178, -1, 0
	v_mbcnt_hi_u32_b32 v178, -1, v178
	v_and_b32_e32 v179, 60, v178
	v_lshlrev_b32_e32 v179, 10, v179
	v_and_b32_e32 v180, 3, v178
	v_lshl_or_b32 v179, v180, 4, v179
	v_add_u32_e32 v180, 0x400, v179
	v_add_u32_e32 v181, 0x800, v179
	v_add_u32_e32 v190, 0xc00, v179
	v_lshlrev_b32_e32 v178, 2, v178
	s_sub_i32 s23, s98, 2048
	s_cmp_lt_u32 s23, 16384
	s_cbranch_scc0 .Lhw_dn_b
	s_lshr_b32 s29, s23, 9
	s_bfe_u32 s24, s23, 0x40005
	s_and_b32 s25, s23, 31
	s_lshl_b32 s30, s29, 23
	s_lshl_b32 s32, s24, 19
	s_add_i32 s30, s30, s32
	s_lshl_b32 s32, s25, 8
	s_add_i32 s30, s30, s32
	s_lshl_b32 s31, s29, 11
	s_bfe_u32 s32, s25, 0x30001
	s_lshl_b32 s32, s32, 8
	s_add_i32 s31, s31, s32
	s_lshr_b32 s32, s25, 4
	s_lshl_b32 s32, s32, 7
	s_add_i32 s31, s31, s32
	s_and_b32 s32, s25, 1
	s_lshl_b32 s32, s32, 6
	s_add_i32 s31, s31, s32
	s_lshl_b32 s31, s31, 10
	s_lshl_b32 s32, s24, 6
	s_add_i32 s31, s31, s32
	s_add_i32 s31, s31, 0x2000000
	v_readlane_b32 s82, v239, 11
	v_readlane_b32 s83, v239, 12
	s_movk_i32 s97, 8192
	s_branch .Lhw_go_b

.Lhw_go_b:
	s_add_u32 s100, s82, s30
	s_addc_u32 s101, s83, 0
	v_readlane_b32 s70, v239, 44
	v_readlane_b32 s71, v239, 45
	s_add_u32 s70, s70, s31
	s_addc_u32 s71, s71, 0
	global_load_dword v34, v178, s[100:101] nt
	s_add_u32 s100, s100, s97
	s_addc_u32 s101, s101, 0
	global_load_dword v35, v178, s[100:101] nt
	s_add_u32 s100, s100, s97
	s_addc_u32 s101, s101, 0
	global_load_dword v36, v178, s[100:101] nt
	s_add_u32 s100, s100, s97
	s_addc_u32 s101, s101, 0
	global_load_dword v37, v178, s[100:101] nt
	s_add_u32 s100, s100, s97
	s_addc_u32 s101, s101, 0
	global_load_dword v38, v178, s[100:101] nt
	s_add_u32 s100, s100, s97
	s_addc_u32 s101, s101, 0
	global_load_dword v39, v178, s[100:101] nt
	s_add_u32 s100, s100, s97
	s_addc_u32 s101, s101, 0
	global_load_dword v40, v178, s[100:101] nt
	s_add_u32 s100, s100, s97
	s_addc_u32 s101, s101, 0
	global_load_dword v41, v178, s[100:101] nt
	s_add_u32 s100, s100, s97
	s_addc_u32 s101, s101, 0
	global_load_dword v42, v178, s[100:101] nt
	s_add_u32 s100, s100, s97
	s_addc_u32 s101, s101, 0
	global_load_dword v43, v178, s[100:101] nt
	s_add_u32 s100, s100, s97
	s_addc_u32 s101, s101, 0
	global_load_dword v44, v178, s[100:101] nt
	s_add_u32 s100, s100, s97
	s_addc_u32 s101, s101, 0
	global_load_dword v45, v178, s[100:101] nt
	s_add_u32 s100, s100, s97
	s_addc_u32 s101, s101, 0
	global_load_dword v46, v178, s[100:101] nt
	s_add_u32 s100, s100, s97
	s_addc_u32 s101, s101, 0
	global_load_dword v47, v178, s[100:101] nt
	s_add_u32 s100, s100, s97
	s_addc_u32 s101, s101, 0
	global_load_dword v48, v178, s[100:101] nt
	s_add_u32 s100, s100, s97
	s_addc_u32 s101, s101, 0
	global_load_dword v49, v178, s[100:101] nt
	s_add_u32 s100, s100, s97
	s_addc_u32 s101, s101, 0
	global_load_dword v50, v178, s[100:101] nt
	s_add_u32 s100, s100, s97
	s_addc_u32 s101, s101, 0
	global_load_dword v51, v178, s[100:101] nt
	s_add_u32 s100, s100, s97
	s_addc_u32 s101, s101, 0
	global_load_dword v52, v178, s[100:101] nt
	s_add_u32 s100, s100, s97
	s_addc_u32 s101, s101, 0
	global_load_dword v53, v178, s[100:101] nt
	s_add_u32 s100, s100, s97
	s_addc_u32 s101, s101, 0
	global_load_dword v54, v178, s[100:101] nt
	s_add_u32 s100, s100, s97
	s_addc_u32 s101, s101, 0
	global_load_dword v55, v178, s[100:101] nt
	s_add_u32 s100, s100, s97
	s_addc_u32 s101, s101, 0
	global_load_dword v56, v178, s[100:101] nt
	s_add_u32 s100, s100, s97
	s_addc_u32 s101, s101, 0
	global_load_dword v57, v178, s[100:101] nt
	s_add_u32 s100, s100, s97
	s_addc_u32 s101, s101, 0
	global_load_dword v58, v178, s[100:101] nt
	s_add_u32 s100, s100, s97
	s_addc_u32 s101, s101, 0
	global_load_dword v59, v178, s[100:101] nt
	s_add_u32 s100, s100, s97
	s_addc_u32 s101, s101, 0
	global_load_dword v60, v178, s[100:101] nt
	s_add_u32 s100, s100, s97
	s_addc_u32 s101, s101, 0
	global_load_dword v61, v178, s[100:101] nt
	s_add_u32 s100, s100, s97
	s_addc_u32 s101, s101, 0
	global_load_dword v62, v178, s[100:101] nt
	s_add_u32 s100, s100, s97
	s_addc_u32 s101, s101, 0
	global_load_dword v63, v178, s[100:101] nt
	s_add_u32 s100, s100, s97
	s_addc_u32 s101, s101, 0
	global_load_dword v64, v178, s[100:101] nt
	s_add_u32 s100, s100, s97
	s_addc_u32 s101, s101, 0
	global_load_dword v65, v178, s[100:101] nt
	s_add_u32 s100, s100, s97
	s_addc_u32 s101, s101, 0
	global_load_dword v66, v178, s[100:101] nt
	s_add_u32 s100, s100, s97
	s_addc_u32 s101, s101, 0
	global_load_dword v67, v178, s[100:101] nt
	s_add_u32 s100, s100, s97
	s_addc_u32 s101, s101, 0
	global_load_dword v68, v178, s[100:101] nt
	s_add_u32 s100, s100, s97
	s_addc_u32 s101, s101, 0
	global_load_dword v69, v178, s[100:101] nt
	s_add_u32 s100, s100, s97
	s_addc_u32 s101, s101, 0
	global_load_dword v70, v178, s[100:101] nt
	s_add_u32 s100, s100, s97
	s_addc_u32 s101, s101, 0
	global_load_dword v71, v178, s[100:101] nt
	s_add_u32 s100, s100, s97
	s_addc_u32 s101, s101, 0
	global_load_dword v72, v178, s[100:101] nt
	s_add_u32 s100, s100, s97
	s_addc_u32 s101, s101, 0
	global_load_dword v73, v178, s[100:101] nt
	s_add_u32 s100, s100, s97
	s_addc_u32 s101, s101, 0
	global_load_dword v74, v178, s[100:101] nt
	s_add_u32 s100, s100, s97
	s_addc_u32 s101, s101, 0
	global_load_dword v75, v178, s[100:101] nt
	s_add_u32 s100, s100, s97
	s_addc_u32 s101, s101, 0
	global_load_dword v76, v178, s[100:101] nt
	s_add_u32 s100, s100, s97
	s_addc_u32 s101, s101, 0
	global_load_dword v77, v178, s[100:101] nt
	s_add_u32 s100, s100, s97
	s_addc_u32 s101, s101, 0
	global_load_dword v78, v178, s[100:101] nt
	s_add_u32 s100, s100, s97
	s_addc_u32 s101, s101, 0
	global_load_dword v79, v178, s[100:101] nt
	s_add_u32 s100, s100, s97
	s_addc_u32 s101, s101, 0
	global_load_dword v80, v178, s[100:101] nt
	s_add_u32 s100, s100, s97
	s_addc_u32 s101, s101, 0
	global_load_dword v81, v178, s[100:101] nt
	s_add_u32 s100, s100, s97
	s_addc_u32 s101, s101, 0
	global_load_dword v82, v178, s[100:101] nt
	s_add_u32 s100, s100, s97
	s_addc_u32 s101, s101, 0
	global_load_dword v83, v178, s[100:101] nt
	s_add_u32 s100, s100, s97
	s_addc_u32 s101, s101, 0
	global_load_dword v84, v178, s[100:101] nt
	s_add_u32 s100, s100, s97
	s_addc_u32 s101, s101, 0
	global_load_dword v85, v178, s[100:101] nt
	s_add_u32 s100, s100, s97
	s_addc_u32 s101, s101, 0
	global_load_dword v86, v178, s[100:101] nt
	s_add_u32 s100, s100, s97
	s_addc_u32 s101, s101, 0
	global_load_dword v87, v178, s[100:101] nt
	s_add_u32 s100, s100, s97
	s_addc_u32 s101, s101, 0
	global_load_dword v88, v178, s[100:101] nt
	s_add_u32 s100, s100, s97
	s_addc_u32 s101, s101, 0
	global_load_dword v89, v178, s[100:101] nt
	s_add_u32 s100, s100, s97
	s_addc_u32 s101, s101, 0
	global_load_dword v90, v178, s[100:101] nt
	s_add_u32 s100, s100, s97
	s_addc_u32 s101, s101, 0
	global_load_dword v91, v178, s[100:101] nt
	s_add_u32 s100, s100, s97
	s_addc_u32 s101, s101, 0
	global_load_dword v92, v178, s[100:101] nt
	s_add_u32 s100, s100, s97
	s_addc_u32 s101, s101, 0
	global_load_dword v93, v178, s[100:101] nt
	s_add_u32 s100, s100, s97
	s_addc_u32 s101, s101, 0
	global_load_dword v94, v178, s[100:101] nt
	s_add_u32 s100, s100, s97
	s_addc_u32 s101, s101, 0
	global_load_dword v95, v178, s[100:101] nt
	s_add_u32 s100, s100, s97
	s_addc_u32 s101, s101, 0
	global_load_dword v96, v178, s[100:101] nt
	s_add_u32 s100, s100, s97
	s_addc_u32 s101, s101, 0
	global_load_dword v97, v178, s[100:101] nt
	s_add_u32 s100, s100, s97
	s_addc_u32 s101, s101, 0
	s_waitcnt vmcnt(48)
	v_mul_f32_e32 v34, 0x42000000, v34
	v_mul_f32_e32 v35, 0x42000000, v35
	v_mul_f32_e32 v36, 0x42000000, v36
	v_mul_f32_e32 v37, 0x42000000, v37
	v_mul_f32_e32 v38, 0x42000000, v38
	v_mul_f32_e32 v39, 0x42000000, v39
	v_mul_f32_e32 v40, 0x42000000, v40
	v_mul_f32_e32 v41, 0x42000000, v41
	v_mul_f32_e32 v42, 0x42000000, v42
	v_mul_f32_e32 v43, 0x42000000, v43
	v_mul_f32_e32 v44, 0x42000000, v44
	v_mul_f32_e32 v45, 0x42000000, v45
	v_mul_f32_e32 v46, 0x42000000, v46
	v_mul_f32_e32 v47, 0x42000000, v47
	v_mul_f32_e32 v48, 0x42000000, v48
	v_mul_f32_e32 v49, 0x42000000, v49
	v_cvt_pk_fp8_f32 v154, v34, v35
	v_cvt_pk_fp8_f32 v155, v38, v39
	v_cvt_pk_fp8_f32 v156, v42, v43
	v_cvt_pk_fp8_f32 v157, v46, v47
	v_cvt_pk_fp8_f32 v154, v36, v37 op_sel:[0,0,1]
	v_cvt_pk_fp8_f32 v155, v40, v41 op_sel:[0,0,1]
	v_cvt_pk_fp8_f32 v156, v44, v45 op_sel:[0,0,1]
	v_cvt_pk_fp8_f32 v157, v48, v49 op_sel:[0,0,1]
	s_waitcnt vmcnt(32)
	v_mul_f32_e32 v50, 0x42000000, v50
	v_mul_f32_e32 v51, 0x42000000, v51
	v_mul_f32_e32 v52, 0x42000000, v52
	v_mul_f32_e32 v53, 0x42000000, v53
	v_mul_f32_e32 v54, 0x42000000, v54
	v_mul_f32_e32 v55, 0x42000000, v55
	v_mul_f32_e32 v56, 0x42000000, v56
	v_mul_f32_e32 v57, 0x42000000, v57
	v_mul_f32_e32 v58, 0x42000000, v58
	v_mul_f32_e32 v59, 0x42000000, v59
	v_mul_f32_e32 v60, 0x42000000, v60
	v_mul_f32_e32 v61, 0x42000000, v61
	v_mul_f32_e32 v62, 0x42000000, v62
	v_mul_f32_e32 v63, 0x42000000, v63
	v_mul_f32_e32 v64, 0x42000000, v64
	v_mul_f32_e32 v65, 0x42000000, v65
	v_cvt_pk_fp8_f32 v158, v50, v51
	v_cvt_pk_fp8_f32 v159, v54, v55
	v_cvt_pk_fp8_f32 v160, v58, v59
	v_cvt_pk_fp8_f32 v161, v62, v63
	v_cvt_pk_fp8_f32 v158, v52, v53 op_sel:[0,0,1]
	v_cvt_pk_fp8_f32 v159, v56, v57 op_sel:[0,0,1]
	v_cvt_pk_fp8_f32 v160, v60, v61 op_sel:[0,0,1]
	v_cvt_pk_fp8_f32 v161, v64, v65 op_sel:[0,0,1]
	s_waitcnt vmcnt(16)
	v_mul_f32_e32 v66, 0x42000000, v66
	v_mul_f32_e32 v67, 0x42000000, v67
	v_mul_f32_e32 v68, 0x42000000, v68
	v_mul_f32_e32 v69, 0x42000000, v69
	v_mul_f32_e32 v70, 0x42000000, v70
	v_mul_f32_e32 v71, 0x42000000, v71
	v_mul_f32_e32 v72, 0x42000000, v72
	v_mul_f32_e32 v73, 0x42000000, v73
	v_mul_f32_e32 v74, 0x42000000, v74
	v_mul_f32_e32 v75, 0x42000000, v75
	v_mul_f32_e32 v76, 0x42000000, v76
	v_mul_f32_e32 v77, 0x42000000, v77
	v_mul_f32_e32 v78, 0x42000000, v78
	v_mul_f32_e32 v79, 0x42000000, v79
	v_mul_f32_e32 v80, 0x42000000, v80
	v_mul_f32_e32 v81, 0x42000000, v81
	v_cvt_pk_fp8_f32 v162, v66, v67
	v_cvt_pk_fp8_f32 v163, v70, v71
	v_cvt_pk_fp8_f32 v164, v74, v75
	v_cvt_pk_fp8_f32 v165, v78, v79
	v_cvt_pk_fp8_f32 v162, v68, v69 op_sel:[0,0,1]
	v_cvt_pk_fp8_f32 v163, v72, v73 op_sel:[0,0,1]
	v_cvt_pk_fp8_f32 v164, v76, v77 op_sel:[0,0,1]
	v_cvt_pk_fp8_f32 v165, v80, v81 op_sel:[0,0,1]
	s_waitcnt vmcnt(0)
	v_mul_f32_e32 v82, 0x42000000, v82
	v_mul_f32_e32 v83, 0x42000000, v83
	v_mul_f32_e32 v84, 0x42000000, v84
	v_mul_f32_e32 v85, 0x42000000, v85
	v_mul_f32_e32 v86, 0x42000000, v86
	v_mul_f32_e32 v87, 0x42000000, v87
	v_mul_f32_e32 v88, 0x42000000, v88
	v_mul_f32_e32 v89, 0x42000000, v89
	v_mul_f32_e32 v90, 0x42000000, v90
	v_mul_f32_e32 v91, 0x42000000, v91
	v_mul_f32_e32 v92, 0x42000000, v92
	v_mul_f32_e32 v93, 0x42000000, v93
	v_mul_f32_e32 v94, 0x42000000, v94
	v_mul_f32_e32 v95, 0x42000000, v95
	v_mul_f32_e32 v96, 0x42000000, v96
	v_mul_f32_e32 v97, 0x42000000, v97
	v_cvt_pk_fp8_f32 v166, v82, v83
	v_cvt_pk_fp8_f32 v167, v86, v87
	v_cvt_pk_fp8_f32 v168, v90, v91
	v_cvt_pk_fp8_f32 v169, v94, v95
	v_cvt_pk_fp8_f32 v166, v84, v85 op_sel:[0,0,1]
	v_cvt_pk_fp8_f32 v167, v88, v89 op_sel:[0,0,1]
	v_cvt_pk_fp8_f32 v168, v92, v93 op_sel:[0,0,1]
	v_cvt_pk_fp8_f32 v169, v96, v97 op_sel:[0,0,1]
	s_mov_b32 vcc_lo, 0xaaaaaaaa
	s_mov_b32 vcc_hi, 0xaaaaaaaa
	s_nop 1
	v_cndmask_b32_dpp v170, v154, v158, vcc quad_perm:[1,0,3,2] row_mask:0xf bank_mask:0xf
	v_cndmask_b32_dpp v174, v162, v166, vcc quad_perm:[1,0,3,2] row_mask:0xf bank_mask:0xf
	v_cndmask_b32_dpp v171, v155, v159, vcc quad_perm:[1,0,3,2] row_mask:0xf bank_mask:0xf
	v_cndmask_b32_dpp v175, v163, v167, vcc quad_perm:[1,0,3,2] row_mask:0xf bank_mask:0xf
	v_cndmask_b32_dpp v172, v156, v160, vcc quad_perm:[1,0,3,2] row_mask:0xf bank_mask:0xf
	v_cndmask_b32_dpp v176, v164, v168, vcc quad_perm:[1,0,3,2] row_mask:0xf bank_mask:0xf
	v_cndmask_b32_dpp v173, v157, v161, vcc quad_perm:[1,0,3,2] row_mask:0xf bank_mask:0xf
	v_cndmask_b32_dpp v177, v165, v169, vcc quad_perm:[1,0,3,2] row_mask:0xf bank_mask:0xf
	s_mov_b32 vcc_lo, 0x55555555
	s_mov_b32 vcc_hi, 0x55555555
	s_nop 1
	v_cndmask_b32_dpp v154, v158, v154, vcc quad_perm:[1,0,3,2] row_mask:0xf bank_mask:0xf
	v_cndmask_b32_dpp v162, v166, v162, vcc quad_perm:[1,0,3,2] row_mask:0xf bank_mask:0xf
	v_cndmask_b32_dpp v155, v159, v155, vcc quad_perm:[1,0,3,2] row_mask:0xf bank_mask:0xf
	v_cndmask_b32_dpp v163, v167, v163, vcc quad_perm:[1,0,3,2] row_mask:0xf bank_mask:0xf
	v_cndmask_b32_dpp v156, v160, v156, vcc quad_perm:[1,0,3,2] row_mask:0xf bank_mask:0xf
	v_cndmask_b32_dpp v164, v168, v164, vcc quad_perm:[1,0,3,2] row_mask:0xf bank_mask:0xf
	v_cndmask_b32_dpp v157, v161, v157, vcc quad_perm:[1,0,3,2] row_mask:0xf bank_mask:0xf
	v_cndmask_b32_dpp v165, v169, v165, vcc quad_perm:[1,0,3,2] row_mask:0xf bank_mask:0xf
	s_mov_b32 vcc_lo, 0xcccccccc
	s_mov_b32 vcc_hi, 0xcccccccc
	s_nop 1
	v_cndmask_b32_dpp v158, v154, v162, vcc quad_perm:[2,3,0,1] row_mask:0xf bank_mask:0xf
	v_cndmask_b32_dpp v166, v170, v174, vcc quad_perm:[2,3,0,1] row_mask:0xf bank_mask:0xf
	v_cndmask_b32_dpp v159, v155, v163, vcc quad_perm:[2,3,0,1] row_mask:0xf bank_mask:0xf
	v_cndmask_b32_dpp v167, v171, v175, vcc quad_perm:[2,3,0,1] row_mask:0xf bank_mask:0xf
	v_cndmask_b32_dpp v160, v156, v164, vcc quad_perm:[2,3,0,1] row_mask:0xf bank_mask:0xf
	v_cndmask_b32_dpp v168, v172, v176, vcc quad_perm:[2,3,0,1] row_mask:0xf bank_mask:0xf
	v_cndmask_b32_dpp v161, v157, v165, vcc quad_perm:[2,3,0,1] row_mask:0xf bank_mask:0xf
	v_cndmask_b32_dpp v169, v173, v177, vcc quad_perm:[2,3,0,1] row_mask:0xf bank_mask:0xf
	s_mov_b32 vcc_lo, 0x33333333
	s_mov_b32 vcc_hi, 0x33333333
	s_nop 1
	v_cndmask_b32_dpp v154, v162, v154, vcc quad_perm:[2,3,0,1] row_mask:0xf bank_mask:0xf
	v_cndmask_b32_dpp v170, v174, v170, vcc quad_perm:[2,3,0,1] row_mask:0xf bank_mask:0xf
	v_cndmask_b32_dpp v155, v163, v155, vcc quad_perm:[2,3,0,1] row_mask:0xf bank_mask:0xf
	v_cndmask_b32_dpp v171, v175, v171, vcc quad_perm:[2,3,0,1] row_mask:0xf bank_mask:0xf
	v_cndmask_b32_dpp v156, v164, v156, vcc quad_perm:[2,3,0,1] row_mask:0xf bank_mask:0xf
	v_cndmask_b32_dpp v172, v176, v172, vcc quad_perm:[2,3,0,1] row_mask:0xf bank_mask:0xf
	v_cndmask_b32_dpp v157, v165, v157, vcc quad_perm:[2,3,0,1] row_mask:0xf bank_mask:0xf
	v_cndmask_b32_dpp v173, v177, v173, vcc quad_perm:[2,3,0,1] row_mask:0xf bank_mask:0xf
	global_store_dwordx4 v179, v[154:157], s[70:71] nt
	global_store_dwordx4 v180, v[170:173], s[70:71] nt
	global_store_dwordx4 v181, v[158:161], s[70:71] nt
	global_store_dwordx4 v190, v[166:169], s[70:71] nt
	s_lshl_b32 s23, s74, 3
	s_add_i32 s98, s98, s23
	s_branch .Lhw_tail

.Lhw_seam0:
	s_mov_b64 exec, -1
	s_cmp_gt_u32 s98, 26623
	s_cbranch_scc1 .Lhw_seam0_done
	v_mbcnt_lo_u32_b32 v178, -1, 0
	v_mbcnt_hi_u32_b32 v178, -1, v178
	v_and_b32_e32 v179, 60, v178
	v_lshlrev_b32_e32 v179, 10, v179
	v_and_b32_e32 v180, 3, v178
	v_lshl_or_b32 v179, v180, 4, v179
	v_add_u32_e32 v180, 0x400, v179
	v_add_u32_e32 v181, 0x800, v179
	v_add_u32_e32 v190, 0xc00, v179
	v_lshlrev_b32_e32 v178, 2, v178
	s_sub_i32 s2, s98, 2048
	s_cmp_lt_u32 s2, 16384
	s_cbranch_scc0 .Lhw_dn_s0_0
	s_lshr_b32 s9, s2, 9
	s_bfe_u32 s32, s2, 0x40005
	s_and_b32 s53, s2, 31
	s_lshl_b32 s69, s9, 23
	s_lshl_b32 s100, s32, 19
	s_add_i32 s69, s69, s100
	s_lshl_b32 s100, s53, 8
	s_add_i32 s69, s69, s100
	s_lshl_b32 s99, s9, 11
	s_bfe_u32 s100, s53, 0x30001
	s_lshl_b32 s100, s100, 8
	s_add_i32 s99, s99, s100
	s_lshr_b32 s100, s53, 4
	s_lshl_b32 s100, s100, 7
	s_add_i32 s99, s99, s100
	s_and_b32 s100, s53, 1
	s_lshl_b32 s100, s100, 6
	s_add_i32 s99, s99, s100
	s_lshl_b32 s99, s99, 10
	s_lshl_b32 s100, s32, 6
	s_add_i32 s99, s99, s100
	s_add_i32 s99, s99, 0x2000000
	v_readlane_b32 s82, v239, 11
	v_readlane_b32 s83, v239, 12
	s_movk_i32 s89, 8192
	s_branch .Lhw_go_s0_0
.Lhw_dn_s0_0:
	s_sub_i32 s2, s2, 16384
	s_lshr_b32 s9, s2, 8
	s_bfe_u32 s32, s2, 0x40004
	s_and_b32 s53, s2, 15
	s_lshl_b32 s69, s9, 22
	s_lshl_b32 s100, s32, 18
	s_add_i32 s69, s69, s100
	s_lshl_b32 s100, s53, 8
	s_add_i32 s69, s69, s100
	s_lshl_b32 s99, s9, 20
	s_lshl_b32 s100, s53, 16
	s_add_i32 s99, s99, s100
	s_lshl_b32 s100, s32, 6
	s_add_i32 s99, s99, s100
	s_add_i32 s99, s99, 0x6000000
	v_readlane_b32 s82, v239, 15
	v_readlane_b32 s83, v239, 16
	s_movk_i32 s89, 4096
.Lhw_go_s0_0:
	s_add_u32 s100, s82, s69
	s_addc_u32 s101, s83, 0
	v_readlane_b32 s82, v239, 44
	v_readlane_b32 s83, v239, 45
	s_add_u32 s82, s82, s99
	s_addc_u32 s83, s83, 0
	global_load_dword v34, v178, s[100:101] nt
	s_add_u32 s100, s100, s89
	s_addc_u32 s101, s101, 0
	global_load_dword v35, v178, s[100:101] nt
	s_add_u32 s100, s100, s89
	s_addc_u32 s101, s101, 0
	global_load_dword v36, v178, s[100:101] nt
	s_add_u32 s100, s100, s89
	s_addc_u32 s101, s101, 0
	global_load_dword v37, v178, s[100:101] nt
	s_add_u32 s100, s100, s89
	s_addc_u32 s101, s101, 0
	global_load_dword v38, v178, s[100:101] nt
	s_add_u32 s100, s100, s89
	s_addc_u32 s101, s101, 0
	global_load_dword v39, v178, s[100:101] nt
	s_add_u32 s100, s100, s89
	s_addc_u32 s101, s101, 0
	global_load_dword v40, v178, s[100:101] nt
	s_add_u32 s100, s100, s89
	s_addc_u32 s101, s101, 0
	global_load_dword v41, v178, s[100:101] nt
	s_add_u32 s100, s100, s89
	s_addc_u32 s101, s101, 0
	global_load_dword v42, v178, s[100:101] nt
	s_add_u32 s100, s100, s89
	s_addc_u32 s101, s101, 0
	global_load_dword v43, v178, s[100:101] nt
	s_add_u32 s100, s100, s89
	s_addc_u32 s101, s101, 0
	global_load_dword v44, v178, s[100:101] nt
	s_add_u32 s100, s100, s89
	s_addc_u32 s101, s101, 0
	global_load_dword v45, v178, s[100:101] nt
	s_add_u32 s100, s100, s89
	s_addc_u32 s101, s101, 0
	global_load_dword v46, v178, s[100:101] nt
	s_add_u32 s100, s100, s89
	s_addc_u32 s101, s101, 0
	global_load_dword v47, v178, s[100:101] nt
	s_add_u32 s100, s100, s89
	s_addc_u32 s101, s101, 0
	global_load_dword v48, v178, s[100:101] nt
	s_add_u32 s100, s100, s89
	s_addc_u32 s101, s101, 0
	global_load_dword v49, v178, s[100:101] nt
	s_add_u32 s100, s100, s89
	s_addc_u32 s101, s101, 0
	global_load_dword v50, v178, s[100:101] nt
	s_add_u32 s100, s100, s89
	s_addc_u32 s101, s101, 0
	global_load_dword v51, v178, s[100:101] nt
	s_add_u32 s100, s100, s89
	s_addc_u32 s101, s101, 0
	global_load_dword v52, v178, s[100:101] nt
	s_add_u32 s100, s100, s89
	s_addc_u32 s101, s101, 0
	global_load_dword v53, v178, s[100:101] nt
	s_add_u32 s100, s100, s89
	s_addc_u32 s101, s101, 0
	global_load_dword v54, v178, s[100:101] nt
	s_add_u32 s100, s100, s89
	s_addc_u32 s101, s101, 0
	global_load_dword v55, v178, s[100:101] nt
	s_add_u32 s100, s100, s89
	s_addc_u32 s101, s101, 0
	global_load_dword v56, v178, s[100:101] nt
	s_add_u32 s100, s100, s89
	s_addc_u32 s101, s101, 0
	global_load_dword v57, v178, s[100:101] nt
	s_add_u32 s100, s100, s89
	s_addc_u32 s101, s101, 0
	global_load_dword v58, v178, s[100:101] nt
	s_add_u32 s100, s100, s89
	s_addc_u32 s101, s101, 0
	global_load_dword v59, v178, s[100:101] nt
	s_add_u32 s100, s100, s89
	s_addc_u32 s101, s101, 0
	global_load_dword v60, v178, s[100:101] nt
	s_add_u32 s100, s100, s89
	s_addc_u32 s101, s101, 0
	global_load_dword v61, v178, s[100:101] nt
	s_add_u32 s100, s100, s89
	s_addc_u32 s101, s101, 0
	global_load_dword v62, v178, s[100:101] nt
	s_add_u32 s100, s100, s89
	s_addc_u32 s101, s101, 0
	global_load_dword v63, v178, s[100:101] nt
	s_add_u32 s100, s100, s89
	s_addc_u32 s101, s101, 0
	global_load_dword v64, v178, s[100:101] nt
	s_add_u32 s100, s100, s89
	s_addc_u32 s101, s101, 0
	global_load_dword v65, v178, s[100:101] nt
	s_add_u32 s100, s100, s89
	s_addc_u32 s101, s101, 0
	global_load_dword v66, v178, s[100:101] nt
	s_add_u32 s100, s100, s89
	s_addc_u32 s101, s101, 0
	global_load_dword v67, v178, s[100:101] nt
	s_add_u32 s100, s100, s89
	s_addc_u32 s101, s101, 0
	global_load_dword v68, v178, s[100:101] nt
	s_add_u32 s100, s100, s89
	s_addc_u32 s101, s101, 0
	global_load_dword v69, v178, s[100:101] nt
	s_add_u32 s100, s100, s89
	s_addc_u32 s101, s101, 0
	global_load_dword v70, v178, s[100:101] nt
	s_add_u32 s100, s100, s89
	s_addc_u32 s101, s101, 0
	global_load_dword v71, v178, s[100:101] nt
	s_add_u32 s100, s100, s89
	s_addc_u32 s101, s101, 0
	global_load_dword v72, v178, s[100:101] nt
	s_add_u32 s100, s100, s89
	s_addc_u32 s101, s101, 0
	global_load_dword v73, v178, s[100:101] nt
	s_add_u32 s100, s100, s89
	s_addc_u32 s101, s101, 0
	global_load_dword v74, v178, s[100:101] nt
	s_add_u32 s100, s100, s89
	s_addc_u32 s101, s101, 0
	global_load_dword v75, v178, s[100:101] nt
	s_add_u32 s100, s100, s89
	s_addc_u32 s101, s101, 0
	global_load_dword v76, v178, s[100:101] nt
	s_add_u32 s100, s100, s89
	s_addc_u32 s101, s101, 0
	global_load_dword v77, v178, s[100:101] nt
	s_add_u32 s100, s100, s89
	s_addc_u32 s101, s101, 0
	global_load_dword v78, v178, s[100:101] nt
	s_add_u32 s100, s100, s89
	s_addc_u32 s101, s101, 0
	global_load_dword v79, v178, s[100:101] nt
	s_add_u32 s100, s100, s89
	s_addc_u32 s101, s101, 0
	global_load_dword v80, v178, s[100:101] nt
	s_add_u32 s100, s100, s89
	s_addc_u32 s101, s101, 0
	global_load_dword v81, v178, s[100:101] nt
	s_add_u32 s100, s100, s89
	s_addc_u32 s101, s101, 0
	global_load_dword v82, v178, s[100:101] nt
	s_add_u32 s100, s100, s89
	s_addc_u32 s101, s101, 0
	global_load_dword v83, v178, s[100:101] nt
	s_add_u32 s100, s100, s89
	s_addc_u32 s101, s101, 0
	global_load_dword v84, v178, s[100:101] nt
	s_add_u32 s100, s100, s89
	s_addc_u32 s101, s101, 0
	global_load_dword v85, v178, s[100:101] nt
	s_add_u32 s100, s100, s89
	s_addc_u32 s101, s101, 0
	global_load_dword v86, v178, s[100:101] nt
	s_add_u32 s100, s100, s89
	s_addc_u32 s101, s101, 0
	global_load_dword v87, v178, s[100:101] nt
	s_add_u32 s100, s100, s89
	s_addc_u32 s101, s101, 0
	global_load_dword v88, v178, s[100:101] nt
	s_add_u32 s100, s100, s89
	s_addc_u32 s101, s101, 0
	global_load_dword v89, v178, s[100:101] nt
	s_add_u32 s100, s100, s89
	s_addc_u32 s101, s101, 0
	global_load_dword v90, v178, s[100:101] nt
	s_add_u32 s100, s100, s89
	s_addc_u32 s101, s101, 0
	global_load_dword v91, v178, s[100:101] nt
	s_add_u32 s100, s100, s89
	s_addc_u32 s101, s101, 0
	global_load_dword v92, v178, s[100:101] nt
	s_add_u32 s100, s100, s89
	s_addc_u32 s101, s101, 0
	global_load_dword v93, v178, s[100:101] nt
	s_add_u32 s100, s100, s89
	s_addc_u32 s101, s101, 0
	global_load_dword v94, v178, s[100:101] nt
	s_add_u32 s100, s100, s89
	s_addc_u32 s101, s101, 0
	global_load_dword v95, v178, s[100:101] nt
	s_add_u32 s100, s100, s89
	s_addc_u32 s101, s101, 0
	global_load_dword v96, v178, s[100:101] nt
	s_add_u32 s100, s100, s89
	s_addc_u32 s101, s101, 0
	global_load_dword v97, v178, s[100:101] nt
	s_add_u32 s100, s100, s89
	s_addc_u32 s101, s101, 0
	s_waitcnt vmcnt(48)
	v_mul_f32_e32 v34, 0x42000000, v34
	v_mul_f32_e32 v35, 0x42000000, v35
	v_mul_f32_e32 v36, 0x42000000, v36
	v_mul_f32_e32 v37, 0x42000000, v37
	v_mul_f32_e32 v38, 0x42000000, v38
	v_mul_f32_e32 v39, 0x42000000, v39
	v_mul_f32_e32 v40, 0x42000000, v40
	v_mul_f32_e32 v41, 0x42000000, v41
	v_mul_f32_e32 v42, 0x42000000, v42
	v_mul_f32_e32 v43, 0x42000000, v43
	v_mul_f32_e32 v44, 0x42000000, v44
	v_mul_f32_e32 v45, 0x42000000, v45
	v_mul_f32_e32 v46, 0x42000000, v46
	v_mul_f32_e32 v47, 0x42000000, v47
	v_mul_f32_e32 v48, 0x42000000, v48
	v_mul_f32_e32 v49, 0x42000000, v49
	v_cvt_pk_fp8_f32 v154, v34, v35
	v_cvt_pk_fp8_f32 v155, v38, v39
	v_cvt_pk_fp8_f32 v156, v42, v43
	v_cvt_pk_fp8_f32 v157, v46, v47
	v_cvt_pk_fp8_f32 v154, v36, v37 op_sel:[0,0,1]
	v_cvt_pk_fp8_f32 v155, v40, v41 op_sel:[0,0,1]
	v_cvt_pk_fp8_f32 v156, v44, v45 op_sel:[0,0,1]
	v_cvt_pk_fp8_f32 v157, v48, v49 op_sel:[0,0,1]
	s_waitcnt vmcnt(32)
	v_mul_f32_e32 v50, 0x42000000, v50
	v_mul_f32_e32 v51, 0x42000000, v51
	v_mul_f32_e32 v52, 0x42000000, v52
	v_mul_f32_e32 v53, 0x42000000, v53
	v_mul_f32_e32 v54, 0x42000000, v54
	v_mul_f32_e32 v55, 0x42000000, v55
	v_mul_f32_e32 v56, 0x42000000, v56
	v_mul_f32_e32 v57, 0x42000000, v57
	v_mul_f32_e32 v58, 0x42000000, v58
	v_mul_f32_e32 v59, 0x42000000, v59
	v_mul_f32_e32 v60, 0x42000000, v60
	v_mul_f32_e32 v61, 0x42000000, v61
	v_mul_f32_e32 v62, 0x42000000, v62
	v_mul_f32_e32 v63, 0x42000000, v63
	v_mul_f32_e32 v64, 0x42000000, v64
	v_mul_f32_e32 v65, 0x42000000, v65
	v_cvt_pk_fp8_f32 v158, v50, v51
	v_cvt_pk_fp8_f32 v159, v54, v55
	v_cvt_pk_fp8_f32 v160, v58, v59
	v_cvt_pk_fp8_f32 v161, v62, v63
	v_cvt_pk_fp8_f32 v158, v52, v53 op_sel:[0,0,1]
	v_cvt_pk_fp8_f32 v159, v56, v57 op_sel:[0,0,1]
	v_cvt_pk_fp8_f32 v160, v60, v61 op_sel:[0,0,1]
	v_cvt_pk_fp8_f32 v161, v64, v65 op_sel:[0,0,1]
	s_waitcnt vmcnt(16)
	v_mul_f32_e32 v66, 0x42000000, v66
	v_mul_f32_e32 v67, 0x42000000, v67
	v_mul_f32_e32 v68, 0x42000000, v68
	v_mul_f32_e32 v69, 0x42000000, v69
	v_mul_f32_e32 v70, 0x42000000, v70
	v_mul_f32_e32 v71, 0x42000000, v71
	v_mul_f32_e32 v72, 0x42000000, v72
	v_mul_f32_e32 v73, 0x42000000, v73
	v_mul_f32_e32 v74, 0x42000000, v74
	v_mul_f32_e32 v75, 0x42000000, v75
	v_mul_f32_e32 v76, 0x42000000, v76
	v_mul_f32_e32 v77, 0x42000000, v77
	v_mul_f32_e32 v78, 0x42000000, v78
	v_mul_f32_e32 v79, 0x42000000, v79
	v_mul_f32_e32 v80, 0x42000000, v80
	v_mul_f32_e32 v81, 0x42000000, v81
	v_cvt_pk_fp8_f32 v162, v66, v67
	v_cvt_pk_fp8_f32 v163, v70, v71
	v_cvt_pk_fp8_f32 v164, v74, v75
	v_cvt_pk_fp8_f32 v165, v78, v79
	v_cvt_pk_fp8_f32 v162, v68, v69 op_sel:[0,0,1]
	v_cvt_pk_fp8_f32 v163, v72, v73 op_sel:[0,0,1]
	v_cvt_pk_fp8_f32 v164, v76, v77 op_sel:[0,0,1]
	v_cvt_pk_fp8_f32 v165, v80, v81 op_sel:[0,0,1]
	s_waitcnt vmcnt(0)
	v_mul_f32_e32 v82, 0x42000000, v82
	v_mul_f32_e32 v83, 0x42000000, v83
	v_mul_f32_e32 v84, 0x42000000, v84
	v_mul_f32_e32 v85, 0x42000000, v85
	v_mul_f32_e32 v86, 0x42000000, v86
	v_mul_f32_e32 v87, 0x42000000, v87
	v_mul_f32_e32 v88, 0x42000000, v88
	v_mul_f32_e32 v89, 0x42000000, v89
	v_mul_f32_e32 v90, 0x42000000, v90
	v_mul_f32_e32 v91, 0x42000000, v91
	v_mul_f32_e32 v92, 0x42000000, v92
	v_mul_f32_e32 v93, 0x42000000, v93
	v_mul_f32_e32 v94, 0x42000000, v94
	v_mul_f32_e32 v95, 0x42000000, v95
	v_mul_f32_e32 v96, 0x42000000, v96
	v_mul_f32_e32 v97, 0x42000000, v97
	v_cvt_pk_fp8_f32 v166, v82, v83
	v_cvt_pk_fp8_f32 v167, v86, v87
	v_cvt_pk_fp8_f32 v168, v90, v91
	v_cvt_pk_fp8_f32 v169, v94, v95
	v_cvt_pk_fp8_f32 v166, v84, v85 op_sel:[0,0,1]
	v_cvt_pk_fp8_f32 v167, v88, v89 op_sel:[0,0,1]
	v_cvt_pk_fp8_f32 v168, v92, v93 op_sel:[0,0,1]
	v_cvt_pk_fp8_f32 v169, v96, v97 op_sel:[0,0,1]
	s_mov_b32 vcc_lo, 0xaaaaaaaa
	s_mov_b32 vcc_hi, 0xaaaaaaaa
	s_nop 1
	v_cndmask_b32_dpp v170, v154, v158, vcc quad_perm:[1,0,3,2] row_mask:0xf bank_mask:0xf
	v_cndmask_b32_dpp v174, v162, v166, vcc quad_perm:[1,0,3,2] row_mask:0xf bank_mask:0xf
	v_cndmask_b32_dpp v171, v155, v159, vcc quad_perm:[1,0,3,2] row_mask:0xf bank_mask:0xf
	v_cndmask_b32_dpp v175, v163, v167, vcc quad_perm:[1,0,3,2] row_mask:0xf bank_mask:0xf
	v_cndmask_b32_dpp v172, v156, v160, vcc quad_perm:[1,0,3,2] row_mask:0xf bank_mask:0xf
	v_cndmask_b32_dpp v176, v164, v168, vcc quad_perm:[1,0,3,2] row_mask:0xf bank_mask:0xf
	v_cndmask_b32_dpp v173, v157, v161, vcc quad_perm:[1,0,3,2] row_mask:0xf bank_mask:0xf
	v_cndmask_b32_dpp v177, v165, v169, vcc quad_perm:[1,0,3,2] row_mask:0xf bank_mask:0xf
	s_mov_b32 vcc_lo, 0x55555555
	s_mov_b32 vcc_hi, 0x55555555
	s_nop 1
	v_cndmask_b32_dpp v154, v158, v154, vcc quad_perm:[1,0,3,2] row_mask:0xf bank_mask:0xf
	v_cndmask_b32_dpp v162, v166, v162, vcc quad_perm:[1,0,3,2] row_mask:0xf bank_mask:0xf
	v_cndmask_b32_dpp v155, v159, v155, vcc quad_perm:[1,0,3,2] row_mask:0xf bank_mask:0xf
	v_cndmask_b32_dpp v163, v167, v163, vcc quad_perm:[1,0,3,2] row_mask:0xf bank_mask:0xf
	v_cndmask_b32_dpp v156, v160, v156, vcc quad_perm:[1,0,3,2] row_mask:0xf bank_mask:0xf
	v_cndmask_b32_dpp v164, v168, v164, vcc quad_perm:[1,0,3,2] row_mask:0xf bank_mask:0xf
	v_cndmask_b32_dpp v157, v161, v157, vcc quad_perm:[1,0,3,2] row_mask:0xf bank_mask:0xf
	v_cndmask_b32_dpp v165, v169, v165, vcc quad_perm:[1,0,3,2] row_mask:0xf bank_mask:0xf
	s_mov_b32 vcc_lo, 0xcccccccc
	s_mov_b32 vcc_hi, 0xcccccccc
	s_nop 1
	v_cndmask_b32_dpp v158, v154, v162, vcc quad_perm:[2,3,0,1] row_mask:0xf bank_mask:0xf
	v_cndmask_b32_dpp v166, v170, v174, vcc quad_perm:[2,3,0,1] row_mask:0xf bank_mask:0xf
	v_cndmask_b32_dpp v159, v155, v163, vcc quad_perm:[2,3,0,1] row_mask:0xf bank_mask:0xf
	v_cndmask_b32_dpp v167, v171, v175, vcc quad_perm:[2,3,0,1] row_mask:0xf bank_mask:0xf
	v_cndmask_b32_dpp v160, v156, v164, vcc quad_perm:[2,3,0,1] row_mask:0xf bank_mask:0xf
	v_cndmask_b32_dpp v168, v172, v176, vcc quad_perm:[2,3,0,1] row_mask:0xf bank_mask:0xf
	v_cndmask_b32_dpp v161, v157, v165, vcc quad_perm:[2,3,0,1] row_mask:0xf bank_mask:0xf
	v_cndmask_b32_dpp v169, v173, v177, vcc quad_perm:[2,3,0,1] row_mask:0xf bank_mask:0xf
	s_mov_b32 vcc_lo, 0x33333333
	s_mov_b32 vcc_hi, 0x33333333
	s_nop 1
	v_cndmask_b32_dpp v154, v162, v154, vcc quad_perm:[2,3,0,1] row_mask:0xf bank_mask:0xf
	v_cndmask_b32_dpp v170, v174, v170, vcc quad_perm:[2,3,0,1] row_mask:0xf bank_mask:0xf
	v_cndmask_b32_dpp v155, v163, v155, vcc quad_perm:[2,3,0,1] row_mask:0xf bank_mask:0xf
	v_cndmask_b32_dpp v171, v175, v171, vcc quad_perm:[2,3,0,1] row_mask:0xf bank_mask:0xf
	v_cndmask_b32_dpp v156, v164, v156, vcc quad_perm:[2,3,0,1] row_mask:0xf bank_mask:0xf
	v_cndmask_b32_dpp v172, v176, v172, vcc quad_perm:[2,3,0,1] row_mask:0xf bank_mask:0xf
	v_cndmask_b32_dpp v157, v165, v157, vcc quad_perm:[2,3,0,1] row_mask:0xf bank_mask:0xf
	v_cndmask_b32_dpp v173, v177, v173, vcc quad_perm:[2,3,0,1] row_mask:0xf bank_mask:0xf
	global_store_dwordx4 v179, v[154:157], s[82:83] nt
	global_store_dwordx4 v180, v[170:173], s[82:83] nt
	global_store_dwordx4 v181, v[158:161], s[82:83] nt
	global_store_dwordx4 v190, v[166:169], s[82:83] nt
	s_lshl_b32 s2, s74, 3
	s_add_i32 s98, s98, s2
.Lhw_seam0_done:
	s_branch .LBB0_107
